# attention merge loop (Lever 1): one counted vmcnt(24) per register set instead of a single full drain per iteration
# baseline (speedup 1.0000x reference)
.LBB0_889:
	v_and_b32_e32 v146, 0x78, v112
	v_lshlrev_b32_e32 v100, 1, v146
	v_mov_b32_e32 v101, v147
	v_lshl_add_u64 v[110:111], v[150:151], 0, v[100:101]
	v_lshl_add_u64 v[108:109], v[160:161], 0, v[100:101]
	v_add_u32_e32 v100, 0xfffff200, v113
	v_add_u32_e32 v138, 0xffffea00, v113
	s_movk_i32 s68, 0x7800
	v_ashrrev_i32_e32 v106, 4, v100
	v_add_u32_e32 v100, 0xfffff400, v113
	v_add_u32_e32 v101, 0xfffff600, v113
	v_add_u32_e32 v103, 0xfffff800, v113
	v_cmp_gt_i32_e32 vcc, s68, v138
	v_ashrrev_i32_e32 v107, 31, v106
	v_ashrrev_i32_e32 v104, 4, v100
	v_ashrrev_i32_e32 v102, 4, v101
	v_ashrrev_i32_e32 v100, 4, v103
	s_and_saveexec_b64 s[80:81], vcc
	s_cbranch_execz .LBB0_891
	v_lshl_add_u64 v[50:51], v[106:107], 2, v[148:149]
	v_add_co_u32_e32 v52, vcc, 0x2000, v50
	v_mad_i64_i32 v[54:55], s[72:73], v106, s77, v[110:111]
	s_nop 0
	v_addc_co_u32_e32 v53, vcc, 0, v51, vcc
	v_add_co_u32_e32 v56, vcc, 0x4000, v50
	v_ashrrev_i32_e32 v105, 31, v104
	s_nop 0
	v_addc_co_u32_e32 v57, vcc, 0, v51, vcc
	v_add_co_u32_e32 v58, vcc, 0x1000, v54
	v_lshl_add_u64 v[70:71], v[104:105], 2, v[148:149]
	s_nop 0
	v_addc_co_u32_e32 v59, vcc, 0, v55, vcc
	v_add_co_u32_e32 v54, vcc, s33, v54
	v_mad_i64_i32 v[62:63], s[72:73], v104, s77, v[110:111]
	s_nop 0
	v_addc_co_u32_e32 v55, vcc, 0, v55, vcc
	v_add_co_u32_e32 v72, vcc, s33, v70
	v_ashrrev_i32_e32 v103, 31, v102
	s_nop 0
	v_addc_co_u32_e32 v73, vcc, 0, v71, vcc
	v_add_co_u32_e32 v74, vcc, s76, v70
	v_lshl_add_u64 v[82:83], v[102:103], 2, v[148:149]
	s_nop 0
	v_addc_co_u32_e32 v75, vcc, 0, v71, vcc
	v_add_co_u32_e32 v66, vcc, s33, v62
	global_load_dword v126, v[50:51], off
	global_load_dword v127, v[52:53], off
	global_load_dword v128, v[56:57], off
	s_nop 0
	global_load_dwordx4 v[50:53], v[58:59], off
	v_addc_co_u32_e32 v67, vcc, 0, v63, vcc
	v_add_co_u32_e32 v84, vcc, s33, v82
	v_lshlrev_b64 v[56:57], 8, v[106:107]
	s_nop 0
	v_addc_co_u32_e32 v85, vcc, 0, v83, vcc
	v_lshl_add_u64 v[58:59], v[108:109], 0, v[56:57]
	v_lshlrev_b64 v[76:77], 8, v[104:105]
	v_add_co_u32_e32 v86, vcc, s76, v82
	global_load_dwordx4 v[54:57], v[54:55], off
	s_nop 0
	global_load_dwordx4 v[58:61], v[58:59], off
	s_nop 0
	global_load_dwordx4 v[62:65], v[66:67], off offset:-4096
	s_nop 0
	global_load_dwordx4 v[66:69], v[66:67], off
	v_lshl_add_u64 v[76:77], v[108:109], 0, v[76:77]
	global_load_dword v129, v[70:71], off
	global_load_dword v130, v[72:73], off
	global_load_dword v131, v[74:75], off
	s_nop 0
	global_load_dwordx4 v[70:73], v[76:77], off
	v_mad_i64_i32 v[74:75], s[72:73], v102, s77, v[110:111]
	v_addc_co_u32_e32 v87, vcc, 0, v83, vcc
	v_add_co_u32_e32 v78, vcc, s33, v74
	v_lshlrev_b64 v[88:89], 8, v[102:103]
	s_nop 0
	v_addc_co_u32_e32 v79, vcc, 0, v75, vcc
	v_ashrrev_i32_e32 v101, 31, v100
	global_load_dwordx4 v[74:77], v[78:79], off offset:-4096
	s_nop 0
	global_load_dwordx4 v[78:81], v[78:79], off
	v_lshl_add_u64 v[88:89], v[108:109], 0, v[88:89]
	global_load_dword v132, v[82:83], off
	global_load_dword v133, v[84:85], off
	global_load_dword v134, v[86:87], off
	s_nop 0
	global_load_dwordx4 v[82:85], v[88:89], off
	v_lshl_add_u64 v[86:87], v[100:101], 2, v[148:149]
	v_add_co_u32_e32 v88, vcc, s33, v86
	v_mad_i64_i32 v[90:91], s[72:73], v100, s77, v[110:111]
	s_nop 0
	v_addc_co_u32_e32 v89, vcc, 0, v87, vcc
	v_add_co_u32_e32 v92, vcc, 0x4000, v86
	s_nop 1
	v_addc_co_u32_e32 v93, vcc, 0, v87, vcc
	v_add_co_u32_e32 v94, vcc, 0x1000, v90
	s_nop 1
	v_addc_co_u32_e32 v95, vcc, 0, v91, vcc
	global_load_dword v135, v[86:87], off
	global_load_dword v136, v[88:89], off
	global_load_dword v137, v[92:93], off
	s_nop 0
	global_load_dwordx4 v[86:89], v[94:95], off
	v_add_co_u32_e32 v90, vcc, 0x2000, v90
	v_lshlrev_b64 v[92:93], 8, v[100:101]
	s_nop 0
	v_addc_co_u32_e32 v91, vcc, 0, v91, vcc
	v_lshl_add_u64 v[94:95], v[108:109], 0, v[92:93]
	global_load_dwordx4 v[90:93], v[90:91], off
	s_nop 0
	global_load_dwordx4 v[94:97], v[94:95], off
	s_or_b64 exec, exec, s[80:81]
	s_waitcnt vmcnt(24)
	s_branch mkmg_b

mkmg_b:
	v_max3_f32 v101, v119, v120, v117
	v_sub_f32_e32 v103, v119, v101
	v_exp_f32_e32 v140, v103
	v_sub_f32_e32 v103, v120, v101
	v_exp_f32_e32 v103, v103
	v_sub_f32_e32 v101, v117, v101
	v_exp_f32_e32 v141, v101
	v_and_b32_e32 v153, 0xffff0000, v35
	v_add_f32_e32 v101, v140, v103
	v_lshlrev_b32_e32 v154, 16, v36
	v_add_f32_e32 v101, v141, v101
	v_div_scale_f32 v105, s[72:73], v101, v101, 1.0
	v_rcp_f32_e32 v139, v105
	v_and_b32_e32 v155, 0xffff0000, v36
	v_lshlrev_b32_e32 v156, 16, v37
	v_ashrrev_i32_e32 v142, 4, v138
	v_fma_f32 v144, -v105, v139, 1.0
	v_fmac_f32_e32 v139, v144, v139
	v_div_scale_f32 v144, vcc, 1.0, v101, 1.0
	v_mul_f32_e32 v145, v144, v139
	v_fma_f32 v152, -v105, v145, v144
	v_fmac_f32_e32 v145, v152, v139
	v_fma_f32 v105, -v105, v145, v144
	v_div_fmas_f32 v105, v105, v139, v145
	v_div_fixup_f32 v144, v105, v101, 1.0
	v_mul_f32_e32 v101, v103, v144
	v_pk_mul_f32 v[140:141], v[140:141], v[144:145] op_sel_hi:[1,0]
	v_lshlrev_b32_e32 v145, 16, v30
	v_lshlrev_b32_e32 v144, 16, v46
	v_lshlrev_b32_e32 v103, 16, v34
	v_pk_mul_f32 v[144:145], v[140:141], v[144:145]
	v_and_b32_e32 v105, 0xffff0000, v34
	v_fma_f32 v103, v101, v103, v144
	v_add_f32_e32 v103, v103, v145
	v_and_b32_e32 v145, 0xffff0000, v30
	v_and_b32_e32 v144, 0xffff0000, v46
	v_pk_mul_f32 v[144:145], v[140:141], v[144:145]
	v_lshlrev_b32_e32 v139, 16, v35
	v_fma_f32 v105, v101, v105, v144
	v_add_f32_e32 v105, v105, v145
	v_lshlrev_b32_e32 v145, 16, v31
	v_lshlrev_b32_e32 v144, 16, v47
	v_pk_mul_f32 v[144:145], v[140:141], v[144:145]
	v_mov_b32_e32 v152, v147
	v_fma_f32 v139, v101, v139, v144
	v_add_f32_e32 v139, v139, v145
	v_and_b32_e32 v145, 0xffff0000, v31
	v_and_b32_e32 v144, 0xffff0000, v47
	v_cvt_pk_fp8_f32 v152, v103, v105
	v_pk_mul_f32 v[144:145], v[140:141], v[144:145]
	v_ashrrev_i32_e32 v143, 31, v142
	v_fma_f32 v103, v101, v153, v144
	v_add_f32_e32 v103, v103, v145
	v_lshlrev_b32_e32 v145, 16, v32
	v_lshlrev_b32_e32 v144, 16, v48
	v_pk_mul_f32 v[144:145], v[140:141], v[144:145]
	v_cvt_pk_fp8_f32 v152, v139, v103 op_sel:[0,0,1]
	v_fma_f32 v103, v101, v154, v144
	v_add_f32_e32 v103, v103, v145
	v_and_b32_e32 v145, 0xffff0000, v32
	v_and_b32_e32 v144, 0xffff0000, v48
	v_pk_mul_f32 v[144:145], v[140:141], v[144:145]
	v_mov_b32_e32 v153, v147
	v_fma_f32 v105, v101, v155, v144
	v_add_f32_e32 v105, v105, v145
	v_lshlrev_b32_e32 v145, 16, v33
	v_lshlrev_b32_e32 v144, 16, v49
	v_pk_mul_f32 v[144:145], v[140:141], v[144:145]
	v_cvt_pk_fp8_f32 v153, v103, v105
	v_fma_f32 v139, v101, v156, v144
	v_add_f32_e32 v139, v139, v145
	v_and_b32_e32 v145, 0xffff0000, v33
	v_and_b32_e32 v144, 0xffff0000, v49
	v_and_b32_e32 v154, 0xffff0000, v37
	v_pk_mul_f32 v[140:141], v[140:141], v[144:145]
	v_and_b32_e32 v155, 0xffff0000, v20
	v_fma_f32 v101, v101, v154, v140
	v_add_f32_e32 v101, v101, v141
	v_cvt_pk_fp8_f32 v153, v139, v101 op_sel:[0,0,1]
	v_max3_f32 v101, v124, v125, v123
	v_sub_f32_e32 v103, v124, v101
	v_lshlrev_b64 v[140:141], 11, v[142:143]
	v_exp_f32_e32 v142, v103
	v_sub_f32_e32 v103, v125, v101
	v_exp_f32_e32 v103, v103
	v_sub_f32_e32 v101, v123, v101
	v_exp_f32_e32 v143, v101
	v_lshl_add_u64 v[140:141], v[98:99], 0, v[140:141]
	v_add_f32_e32 v101, v142, v103
	v_lshl_add_u64 v[140:141], v[140:141], 0, v[146:147]
	v_add_f32_e32 v101, v143, v101
	v_div_scale_f32 v105, s[72:73], v101, v101, 1.0
	v_rcp_f32_e32 v139, v105
	global_store_dwordx2 v[140:141], v[152:153], off
	v_and_b32_e32 v153, 0xffff0000, v19
	v_lshlrev_b32_e32 v154, 16, v20
	v_fma_f32 v144, -v105, v139, 1.0
	v_fmac_f32_e32 v139, v144, v139
	v_div_scale_f32 v144, vcc, 1.0, v101, 1.0
	v_mul_f32_e32 v145, v144, v139
	v_fma_f32 v152, -v105, v145, v144
	v_fmac_f32_e32 v145, v152, v139
	v_fma_f32 v105, -v105, v145, v144
	v_div_fmas_f32 v105, v105, v139, v145
	v_div_fixup_f32 v144, v105, v101, 1.0
	v_mul_f32_e32 v101, v103, v144
	v_pk_mul_f32 v[142:143], v[142:143], v[144:145] op_sel_hi:[1,0]
	v_lshlrev_b32_e32 v145, 16, v22
	v_lshlrev_b32_e32 v144, 16, v42
	v_lshlrev_b32_e32 v103, 16, v18
	v_pk_mul_f32 v[144:145], v[142:143], v[144:145]
	v_and_b32_e32 v105, 0xffff0000, v18
	v_fma_f32 v103, v101, v103, v144
	v_add_f32_e32 v103, v103, v145
	v_and_b32_e32 v145, 0xffff0000, v22
	v_and_b32_e32 v144, 0xffff0000, v42
	v_pk_mul_f32 v[144:145], v[142:143], v[144:145]
	v_lshlrev_b32_e32 v139, 16, v19
	v_fma_f32 v105, v101, v105, v144
	v_add_f32_e32 v105, v105, v145
	v_lshlrev_b32_e32 v145, 16, v23
	v_lshlrev_b32_e32 v144, 16, v43
	v_pk_mul_f32 v[144:145], v[142:143], v[144:145]
	v_mov_b32_e32 v152, v147
	v_fma_f32 v139, v101, v139, v144
	v_add_f32_e32 v139, v139, v145
	v_and_b32_e32 v145, 0xffff0000, v23
	v_and_b32_e32 v144, 0xffff0000, v43
	v_cvt_pk_fp8_f32 v152, v103, v105
	v_pk_mul_f32 v[144:145], v[142:143], v[144:145]
	v_lshlrev_b32_e32 v156, 16, v21
	v_fma_f32 v103, v101, v153, v144
	v_add_f32_e32 v103, v103, v145
	v_lshlrev_b32_e32 v145, 16, v24
	v_lshlrev_b32_e32 v144, 16, v44
	v_pk_mul_f32 v[144:145], v[142:143], v[144:145]
	v_cvt_pk_fp8_f32 v152, v139, v103 op_sel:[0,0,1]
	v_fma_f32 v103, v101, v154, v144
	v_add_f32_e32 v103, v103, v145
	v_and_b32_e32 v145, 0xffff0000, v24
	v_and_b32_e32 v144, 0xffff0000, v44
	v_pk_mul_f32 v[144:145], v[142:143], v[144:145]
	v_mov_b32_e32 v153, v147
	v_fma_f32 v105, v101, v155, v144
	v_add_f32_e32 v105, v105, v145
	v_lshlrev_b32_e32 v145, 16, v25
	v_lshlrev_b32_e32 v144, 16, v45
	v_pk_mul_f32 v[144:145], v[142:143], v[144:145]
	v_cvt_pk_fp8_f32 v153, v103, v105
	v_fma_f32 v139, v101, v156, v144
	v_add_f32_e32 v139, v139, v145
	v_and_b32_e32 v145, 0xffff0000, v25
	v_and_b32_e32 v144, 0xffff0000, v45
	v_and_b32_e32 v154, 0xffff0000, v21
	v_pk_mul_f32 v[142:143], v[142:143], v[144:145]
	v_add_u32_e32 v140, 0xffffec00, v113
	v_fma_f32 v101, v101, v154, v142
	v_add_f32_e32 v101, v101, v143
	v_cvt_pk_fp8_f32 v153, v139, v101 op_sel:[0,0,1]
	v_max3_f32 v101, v121, v122, v118
	v_sub_f32_e32 v103, v121, v101
	v_exp_f32_e32 v142, v103
	v_sub_f32_e32 v103, v122, v101
	v_exp_f32_e32 v103, v103
	v_sub_f32_e32 v101, v118, v101
	v_exp_f32_e32 v143, v101
	v_ashrrev_i32_e32 v140, 4, v140
	v_add_f32_e32 v101, v142, v103
	v_ashrrev_i32_e32 v141, 31, v140
	v_add_f32_e32 v101, v143, v101
	v_div_scale_f32 v105, s[72:73], v101, v101, 1.0
	v_rcp_f32_e32 v139, v105
	v_lshlrev_b64 v[140:141], 11, v[140:141]
	v_lshl_add_u64 v[140:141], v[98:99], 0, v[140:141]
	v_lshl_add_u64 v[140:141], v[140:141], 0, v[146:147]
	v_fma_f32 v144, -v105, v139, 1.0
	v_fmac_f32_e32 v139, v144, v139
	v_div_scale_f32 v144, vcc, 1.0, v101, 1.0
	v_mul_f32_e32 v145, v144, v139
	global_store_dwordx2 v[140:141], v[152:153], off
	v_fma_f32 v152, -v105, v145, v144
	v_fmac_f32_e32 v145, v152, v139
	v_fma_f32 v105, -v105, v145, v144
	v_div_fmas_f32 v105, v105, v139, v145
	v_div_fixup_f32 v144, v105, v101, 1.0
	v_mul_f32_e32 v101, v103, v144
	v_pk_mul_f32 v[142:143], v[142:143], v[144:145] op_sel_hi:[1,0]
	v_lshlrev_b32_e32 v145, 16, v10
	v_lshlrev_b32_e32 v144, 16, v38
	v_lshlrev_b32_e32 v103, 16, v2
	v_pk_mul_f32 v[144:145], v[142:143], v[144:145]
	v_and_b32_e32 v105, 0xffff0000, v2
	v_fma_f32 v103, v101, v103, v144
	v_add_f32_e32 v103, v103, v145
	v_and_b32_e32 v145, 0xffff0000, v10
	v_and_b32_e32 v144, 0xffff0000, v38
	v_pk_mul_f32 v[144:145], v[142:143], v[144:145]
	v_lshlrev_b32_e32 v139, 16, v3
	v_fma_f32 v105, v101, v105, v144
	v_add_f32_e32 v105, v105, v145
	v_lshlrev_b32_e32 v145, 16, v11
	v_lshlrev_b32_e32 v144, 16, v39
	v_pk_mul_f32 v[144:145], v[142:143], v[144:145]
	v_mov_b32_e32 v152, v147
	v_fma_f32 v139, v101, v139, v144
	v_add_f32_e32 v139, v139, v145
	v_and_b32_e32 v145, 0xffff0000, v11
	v_and_b32_e32 v144, 0xffff0000, v39
	v_and_b32_e32 v153, 0xffff0000, v3
	v_cvt_pk_fp8_f32 v152, v103, v105
	v_pk_mul_f32 v[144:145], v[142:143], v[144:145]
	v_lshlrev_b32_e32 v154, 16, v4
	v_fma_f32 v103, v101, v153, v144
	v_add_f32_e32 v103, v103, v145
	v_lshlrev_b32_e32 v145, 16, v12
	v_lshlrev_b32_e32 v144, 16, v40
	v_pk_mul_f32 v[144:145], v[142:143], v[144:145]
	v_cvt_pk_fp8_f32 v152, v139, v103 op_sel:[0,0,1]
	v_fma_f32 v103, v101, v154, v144
	v_add_f32_e32 v103, v103, v145
	v_and_b32_e32 v145, 0xffff0000, v12
	v_and_b32_e32 v144, 0xffff0000, v40
	v_and_b32_e32 v155, 0xffff0000, v4
	v_pk_mul_f32 v[144:145], v[142:143], v[144:145]
	v_lshlrev_b32_e32 v156, 16, v5
	v_fma_f32 v105, v101, v155, v144
	v_add_f32_e32 v105, v105, v145
	v_lshlrev_b32_e32 v145, 16, v13
	v_lshlrev_b32_e32 v144, 16, v41
	v_pk_mul_f32 v[144:145], v[142:143], v[144:145]
	v_mov_b32_e32 v153, v147
	v_fma_f32 v139, v101, v156, v144
	v_add_f32_e32 v139, v139, v145
	v_and_b32_e32 v145, 0xffff0000, v13
	v_and_b32_e32 v144, 0xffff0000, v41
	v_cvt_pk_fp8_f32 v153, v103, v105
	v_and_b32_e32 v154, 0xffff0000, v5
	v_pk_mul_f32 v[142:143], v[142:143], v[144:145]
	v_add_u32_e32 v140, 0xffffee00, v113
	v_fma_f32 v101, v101, v154, v142
	v_add_f32_e32 v101, v101, v143
	v_cvt_pk_fp8_f32 v153, v139, v101 op_sel:[0,0,1]
	v_max3_f32 v101, v115, v116, v114
	v_sub_f32_e32 v103, v115, v101
	v_exp_f32_e32 v142, v103
	v_sub_f32_e32 v103, v116, v101
	v_exp_f32_e32 v103, v103
	v_sub_f32_e32 v101, v114, v101
	v_exp_f32_e32 v143, v101
	v_ashrrev_i32_e32 v140, 4, v140
	v_add_f32_e32 v101, v142, v103
	v_ashrrev_i32_e32 v141, 31, v140
	v_add_f32_e32 v101, v143, v101
	v_div_scale_f32 v105, s[72:73], v101, v101, 1.0
	v_rcp_f32_e32 v139, v105
	v_lshlrev_b64 v[140:141], 11, v[140:141]
	v_lshl_add_u64 v[140:141], v[98:99], 0, v[140:141]
	v_lshl_add_u64 v[140:141], v[140:141], 0, v[146:147]
	v_fma_f32 v144, -v105, v139, 1.0
	v_fmac_f32_e32 v139, v144, v139
	v_div_scale_f32 v144, vcc, 1.0, v101, 1.0
	v_mul_f32_e32 v145, v144, v139
	global_store_dwordx2 v[140:141], v[152:153], off
	v_fma_f32 v152, -v105, v145, v144
	v_fmac_f32_e32 v145, v152, v139
	v_fma_f32 v105, -v105, v145, v144
	v_div_fmas_f32 v105, v105, v139, v145
	v_div_fixup_f32 v144, v105, v101, 1.0
	v_mul_f32_e32 v101, v103, v144
	v_pk_mul_f32 v[142:143], v[142:143], v[144:145] op_sel_hi:[1,0]
	v_lshlrev_b32_e32 v145, 16, v6
	v_lshlrev_b32_e32 v144, 16, v26
	v_lshlrev_b32_e32 v103, 16, v14
	v_pk_mul_f32 v[144:145], v[142:143], v[144:145]
	v_and_b32_e32 v105, 0xffff0000, v14
	v_fma_f32 v103, v101, v103, v144
	v_add_f32_e32 v103, v103, v145
	v_and_b32_e32 v145, 0xffff0000, v6
	v_and_b32_e32 v144, 0xffff0000, v26
	v_pk_mul_f32 v[144:145], v[142:143], v[144:145]
	v_lshlrev_b32_e32 v139, 16, v15
	v_fma_f32 v105, v101, v105, v144
	v_add_f32_e32 v105, v105, v145
	v_lshlrev_b32_e32 v145, 16, v7
	v_lshlrev_b32_e32 v144, 16, v27
	v_pk_mul_f32 v[144:145], v[142:143], v[144:145]
	v_mov_b32_e32 v152, v147
	v_fma_f32 v139, v101, v139, v144
	v_add_f32_e32 v139, v139, v145
	v_and_b32_e32 v145, 0xffff0000, v7
	v_and_b32_e32 v144, 0xffff0000, v27
	v_and_b32_e32 v153, 0xffff0000, v15
	v_cvt_pk_fp8_f32 v152, v103, v105
	v_pk_mul_f32 v[144:145], v[142:143], v[144:145]
	v_lshlrev_b32_e32 v154, 16, v16
	v_fma_f32 v103, v101, v153, v144
	v_add_f32_e32 v103, v103, v145
	v_lshlrev_b32_e32 v145, 16, v8
	v_lshlrev_b32_e32 v144, 16, v28
	v_pk_mul_f32 v[144:145], v[142:143], v[144:145]
	v_cvt_pk_fp8_f32 v152, v139, v103 op_sel:[0,0,1]
	v_fma_f32 v103, v101, v154, v144
	v_add_f32_e32 v103, v103, v145
	v_and_b32_e32 v145, 0xffff0000, v8
	v_and_b32_e32 v144, 0xffff0000, v28
	v_and_b32_e32 v155, 0xffff0000, v16
	v_pk_mul_f32 v[144:145], v[142:143], v[144:145]
	v_lshlrev_b32_e32 v156, 16, v17
	v_fma_f32 v105, v101, v155, v144
	v_add_f32_e32 v105, v105, v145
	v_lshlrev_b32_e32 v145, 16, v9
	v_lshlrev_b32_e32 v144, 16, v29
	v_pk_mul_f32 v[144:145], v[142:143], v[144:145]
	v_mov_b32_e32 v153, v147
	v_fma_f32 v139, v101, v156, v144
	v_add_f32_e32 v139, v139, v145
	v_and_b32_e32 v145, 0xffff0000, v9
	v_and_b32_e32 v144, 0xffff0000, v29
	v_cvt_pk_fp8_f32 v153, v103, v105
	v_and_b32_e32 v154, 0xffff0000, v17
	v_pk_mul_f32 v[142:143], v[142:143], v[144:145]
	v_add_u32_e32 v140, 0xfffff000, v113
	v_fma_f32 v101, v101, v154, v142
	v_ashrrev_i32_e32 v140, 4, v140
	v_add_f32_e32 v101, v101, v143
	v_ashrrev_i32_e32 v141, 31, v140
	v_cvt_pk_fp8_f32 v153, v139, v101 op_sel:[0,0,1]
	v_lshlrev_b64 v[140:141], 11, v[140:141]
	v_lshl_add_u64 v[140:141], v[98:99], 0, v[140:141]
	s_movk_i32 s68, 0x7000
	v_lshl_add_u64 v[140:141], v[140:141], 0, v[146:147]
	v_cmp_gt_i32_e32 vcc, s68, v138
	global_store_dwordx2 v[140:141], v[152:153], off
	s_and_saveexec_b64 s[80:81], vcc
	s_cbranch_execz mkmg_a0
	v_add_u32_e32 v2, 0xfffffa00, v113
	v_ashrrev_i32_e32 v2, 4, v2
	v_ashrrev_i32_e32 v3, 31, v2
	v_lshl_add_u64 v[6:7], v[2:3], 2, v[148:149]
	v_add_co_u32_e32 v8, vcc, 0x2000, v6
	v_mad_i64_i32 v[4:5], s[72:73], v2, s77, v[110:111]
	s_nop 0
	v_addc_co_u32_e32 v9, vcc, 0, v7, vcc
	v_add_co_u32_e32 v10, vcc, 0x4000, v6
	v_lshlrev_b64 v[2:3], 8, v[2:3]
	s_nop 0
	v_addc_co_u32_e32 v11, vcc, 0, v7, vcc
	v_add_co_u32_e32 v12, vcc, 0x1000, v4
	v_lshl_add_u64 v[2:3], v[108:109], 0, v[2:3]
	s_nop 0
	v_addc_co_u32_e32 v13, vcc, 0, v5, vcc
	v_add_co_u32_e32 v4, vcc, s33, v4
	global_load_dword v119, v[6:7], off
	global_load_dword v120, v[8:9], off
	global_load_dword v117, v[10:11], off
	global_load_dwordx4 v[46:49], v[12:13], off
	v_addc_co_u32_e32 v5, vcc, 0, v5, vcc
	global_load_dwordx4 v[34:37], v[4:5], off
	global_load_dwordx4 v[30:33], v[2:3], off
	v_add_u32_e32 v2, 0xfffffc00, v113
	v_ashrrev_i32_e32 v2, 4, v2
	v_ashrrev_i32_e32 v3, 31, v2
	v_lshl_add_u64 v[6:7], v[2:3], 2, v[148:149]
	v_add_co_u32_e32 v8, vcc, s33, v6
	v_mad_i64_i32 v[4:5], s[72:73], v2, s77, v[110:111]
	s_nop 0
	v_addc_co_u32_e32 v9, vcc, 0, v7, vcc
	v_add_co_u32_e32 v10, vcc, s76, v6
	v_lshlrev_b64 v[2:3], 8, v[2:3]
	s_nop 0
	v_addc_co_u32_e32 v11, vcc, 0, v7, vcc
	v_add_co_u32_e32 v4, vcc, s33, v4
	v_lshl_add_u64 v[2:3], v[108:109], 0, v[2:3]
	s_nop 0
	v_addc_co_u32_e32 v5, vcc, 0, v5, vcc
	global_load_dwordx4 v[42:45], v[4:5], off offset:-4096
	global_load_dwordx4 v[18:21], v[4:5], off
	global_load_dword v124, v[6:7], off
	global_load_dword v125, v[8:9], off
	global_load_dword v123, v[10:11], off
	global_load_dwordx4 v[22:25], v[2:3], off
	v_add_u32_e32 v2, 0xfffffe00, v113
	v_ashrrev_i32_e32 v6, 4, v2
	v_ashrrev_i32_e32 v7, 31, v6
	v_lshl_add_u64 v[8:9], v[6:7], 2, v[148:149]
	v_add_co_u32_e32 v10, vcc, s33, v8
	v_mad_i64_i32 v[2:3], s[72:73], v6, s77, v[110:111]
	s_nop 0
	v_addc_co_u32_e32 v11, vcc, 0, v9, vcc
	v_add_co_u32_e32 v12, vcc, s76, v8
	v_lshlrev_b64 v[6:7], 8, v[6:7]
	s_nop 0
	v_addc_co_u32_e32 v13, vcc, 0, v9, vcc
	v_add_co_u32_e32 v2, vcc, s33, v2
	v_lshl_add_u64 v[6:7], v[108:109], 0, v[6:7]
	s_nop 0
	v_addc_co_u32_e32 v3, vcc, 0, v3, vcc
	global_load_dwordx4 v[38:41], v[2:3], off offset:-4096
	s_nop 0
	global_load_dwordx4 v[2:5], v[2:3], off
	s_nop 0
	global_load_dword v121, v[8:9], off
	global_load_dword v122, v[10:11], off
	global_load_dword v118, v[12:13], off
	s_nop 0
	global_load_dwordx4 v[10:13], v[6:7], off
	v_ashrrev_i32_e32 v6, 4, v113
	v_ashrrev_i32_e32 v7, 31, v6
	v_lshl_add_u64 v[14:15], v[6:7], 2, v[148:149]
	v_add_co_u32_e32 v16, vcc, s33, v14
	v_mad_i64_i32 v[8:9], s[72:73], v6, s77, v[110:111]
	s_nop 0
	v_addc_co_u32_e32 v17, vcc, 0, v15, vcc
	v_add_co_u32_e32 v26, vcc, 0x4000, v14
	v_lshlrev_b64 v[6:7], 8, v[6:7]
	s_nop 0
	v_addc_co_u32_e32 v27, vcc, 0, v15, vcc
	v_add_co_u32_e32 v28, vcc, 0x1000, v8
	v_lshl_add_u64 v[6:7], v[108:109], 0, v[6:7]
	s_nop 0
	v_addc_co_u32_e32 v29, vcc, 0, v9, vcc
	global_load_dword v115, v[14:15], off
	global_load_dword v116, v[16:17], off
	global_load_dword v114, v[26:27], off
	s_nop 0
	global_load_dwordx4 v[26:29], v[28:29], off
	v_add_co_u32_e32 v8, vcc, 0x2000, v8
	s_nop 1
	v_addc_co_u32_e32 v9, vcc, 0, v9, vcc
	global_load_dwordx4 v[14:17], v[8:9], off
	s_nop 0
	global_load_dwordx4 v[6:9], v[6:7], off
	s_waitcnt vmcnt(24)
	s_branch .LBB0_888
mkmg_a0:
	s_waitcnt vmcnt(0)
	s_branch .LBB0_888
